# code placement: the GEMM K-loop / piece-loop heads are 64-byte aligned
# speedup vs baseline: 1.0045x; 1.0045x over previous
; #define PG8_STAGEA(bufoff, uptr, koff, NEXT, h) do { if constexpr (GATHER) { if (NEXT) { const u32x2 _t = *(const LAS u32x2*)(vnslot + 2 * (h)); unsigned _v[2] = {_t.x, _t.y}; PG8_STAGE(bufoff, Abase + (koff), _v); } else { PG8_STAGE(bufoff, Abase + (koff), vc[h]); } } \
;         else { PG8_STAGE(bufoff, (uptr) + (size_t)(h) * hstep + (koff), voffA); } } while (0)
; #define PG8_SCHED __builtin_amdgcn_sched_barrier(0)
;     __device__ __forceinline__ size_t aoff(const Unit& u) const { return (size_t)u.pm * BM * K * 2; }
;     __device__ __forceinline__ size_t aoff(const Unit& u) const { return (size_t)u.pm * BM * K * 2; }
;     ...
;         const char* nB = has_next ? nxt.B : cB; const char* nA = has_next ? Abase + S.aoff(nxt) : cA;
;         const bool fresh_nxt = !(AREUSE && has_next && nxt.e == cur.e && nxt.pm == cur.pm);
;         const bool ff = fresh_cur && fresh_nxt;
;     ...
;         for (int t = 0; t < nt; t += 2) {
;             const bool last = (t == nt - 2);
;             const size_t k1 = (size_t)(t + 1) * kstep;
;             const size_t k2 = last ? (size_t)0 : (size_t)(t + 2) * kstep, k3 = k2 + kstep;
;             const char* u2 = last ? nA : cA; const char* b2 = last ? nB : cB + (size_t)(t + 2) * kstep;
;             const char* b3 = b2 + kstep;
;             PG8_LDB(B0, 0, 0); PG8_LDB(B1, 0, 1); PG8_SCHED; PG8_LDA(At, 0, 0); if (!AREUSE || fresh_cur) PG8_STAGEA(PG8_SA(1, 1), cA, k1, false, 1);
.LBB0_206:
	s_ashr_i32 s23, s22, 31
	s_lshl_b64 s[4:5], s[22:23], 18
	s_add_u32 s26, s33, s4
	s_addc_u32 s27, s38, s5
	s_add_u32 s21, s34, 0x100
	s_addc_u32 s23, s35, 0
	v_lshl_add_u64 v[26:27], s[30:31], 0, v[164:165]
	v_lshl_add_u64 v[172:173], s[30:31], 0, v[166:167]
	s_mov_b32 s53, -2
	s_mov_b64 s[4:5], 0
	.p2align	6

;     __device__ __forceinline__ size_t aoff(const Unit& u) const { return (size_t)u.pm * BM * K * 2; }
;     __device__ __forceinline__ size_t aoff(const Unit& u) const { return (size_t)u.pm * BM * K * 2; }
;     ...
;         const char* nB = has_next ? nxt.B : cB; const char* nA = has_next ? Abase + S.aoff(nxt) : cA;
;         const bool fresh_nxt = !(AREUSE && has_next && nxt.e == cur.e && nxt.pm == cur.pm);
;         const bool ff = fresh_cur && fresh_nxt;
;     ...
;         for (int t = 0; t < nt; t += 2) {
;             const bool last = (t == nt - 2);
;             const size_t k1 = (size_t)(t + 1) * kstep;
;             const size_t k2 = last ? (size_t)0 : (size_t)(t + 2) * kstep, k3 = k2 + kstep;
;             const char* u2 = last ? nA : cA; const char* b2 = last ? nB : cB + (size_t)(t + 2) * kstep;
;             const char* b3 = b2 + kstep;
.LBB0_405:
	s_mov_b32 s13, s64
	s_add_i32 s64, s64, 1
	s_cmp_lt_u32 s13, 3
	s_cselect_b64 s[8:9], -1, 0
	s_lshl_b32 s6, s64, 18
	s_add_i32 s6, s6, s98
	s_and_b32 s6, s6, 0xc0000
	s_add_u32 s20, s24, s6
	s_addc_u32 s21, s25, 0
	s_and_b64 s[6:7], s[8:9], exec
	s_mov_b64 s[4:5], s[30:31]
	s_mov_b32 s65, s92
	s_cselect_b32 s92, s2, s92
	s_cselect_b32 s31, s21, s5
	s_cselect_b32 s30, s20, s4
	s_ashr_i32 s93, s92, 31
	s_lshl_b64 s[6:7], s[92:93], 18
	s_add_u32 s20, s89, s6
	s_addc_u32 s21, s33, s7
	s_mov_b64 vcc, s[96:97]
	s_and_b64 s[6:7], s[8:9], exec
	s_cselect_b32 s97, s21, vcc_hi
	s_cselect_b32 s96, s20, vcc_lo
	s_add_u32 s93, s4, 0x100
	s_addc_u32 s66, s5, 0
	s_add_u32 s4, vcc_lo, 0x20080
	s_addc_u32 s5, vcc_hi, 0
	v_lshl_add_u64 v[26:27], s[4:5], 0, v[170:171]
	v_lshl_add_u64 v[174:175], s[4:5], 0, v[172:173]
	s_mov_b32 s67, -2
	s_mov_b64 s[6:7], 0
	.p2align	6

; #define PG8_STAGE(bufoff, gbase, voff) do { _Pragma("unroll") for (int _i = 0; _i < 2; ++_i) \
;         __builtin_amdgcn_global_load_lds((const unsigned*)((const char*)(gbase) + (voff)[_i]), (LAS unsigned*)(lds + (bufoff) + ldsw + _i * 8192), 16, 0, 0); } while (0)
; #define PG8_STAGEA(bufoff, uptr, koff, NEXT, h) do { if constexpr (GATHER) { if (NEXT) { const u32x2 _t = *(const LAS u32x2*)(vnslot + 2 * (h)); unsigned _v[2] = {_t.x, _t.y}; PG8_STAGE(bufoff, Abase + (koff), _v); } else { PG8_STAGE(bufoff, Abase + (koff), vc[h]); } } \
;         else { PG8_STAGE(bufoff, (uptr) + (size_t)(h) * hstep + (koff), voffA); } } while (0)
; #define PG8_WAIT_V(n) asm volatile("s_waitcnt vmcnt(" #n ")" ::: "memory")
; #define PG8_BAR __builtin_amdgcn_s_barrier()
;     ...
;     PG8_STAGE(PG8_SB(0, 0), cB, voffB); PG8_STAGE(PG8_SB(0, 1), cB + bhstep, voffB); PG8_STAGEA(PG8_SA(0, 0), cA, 0, false, 0); PG8_STAGEA(PG8_SA(0, 1), cA, 0, false, 1);
;     if (wr == 1) PG8_BAR;
;     PG8_WAIT_V(2); PG8_BAR;
;     PG8_STAGE(PG8_SB(1, 0), cB + kstep, voffB); PG8_STAGEA(PG8_SA(1, 0), cA, kstep, false, 0); PG8_STAGE(PG8_SB(1, 1), cB + bhstep + kstep, voffB);
;     PG8_WAIT_V(6); PG8_BAR;
;     asm volatile("" ::: "memory");
; #pragma unroll
;     for (int a = 0; a < 2; ++a)
; #pragma unroll
;         for (int b = 0; b < 2; ++b)
; #pragma unroll
;             for (int m = 0; m < 4; ++m)
; #pragma unroll
;                 for (int n = 0; n < 2; ++n) { acc[a][b][m][n] = (f32x4){0.f, 0.f, 0.f, 0.f}; asm volatile("" : "+v"(acc[a][b][m][n])); }
;     asm volatile("s_nop 4" ::: "memory");
.LBB0_422:
	s_lshl_b32 s4, s4, 5
	v_and_b32_e32 v5, 48, v4
	v_lshlrev_b32_e32 v6, 6, v4
	s_movk_i32 s6, 0x3c0
	v_lshlrev_b32_e32 v4, 2, v4
	s_and_b32 s16, s4, 0x60
	s_lshl_b32 s21, s5, 6
	s_lshl_b32 s5, s5, 13
	v_and_or_b32 v5, v6, s6, v5
	v_and_b32_e32 v4, 32, v4
	s_lshl_b32 s4, s16, 7
	v_bitop3_b32 v144, v5, s5, v4 bitop3:0xde
	v_bitop3_b32 v25, s4, v5, v4 bitop3:0xf6
	v_readlane_b32 s4, v252, 34
	v_readlane_b32 s5, v252, 35
	s_add_i32 m0, s3, 0x18000
	s_waitcnt vmcnt(2)
	s_barrier
	v_lshl_add_u64 v[4:5], s[4:5], 0, v[136:137]
	global_load_lds_dwordx4 v[4:5], off
	v_lshl_add_u64 v[4:5], s[4:5], 0, v[26:27]
	s_add_i32 m0, s3, 0x1a000
	s_add_i32 s56, s3, 0x8000
	global_load_lds_dwordx4 v[4:5], off
	v_lshl_add_u64 v[2:3], v[2:3], 0, s[82:83]
	s_mov_b32 m0, s56
	s_add_i32 s57, s3, 0xa000
	v_readlane_b32 s4, v252, 36
	global_load_lds_dwordx4 v[2:3], off
	v_lshl_add_u64 v[0:1], v[0:1], 0, s[82:83]
	s_mov_b32 m0, s57
	v_readlane_b32 s5, v252, 37
	global_load_lds_dwordx4 v[0:1], off
	s_add_i32 m0, s3, 0x1c000
	v_lshl_add_u64 v[0:1], s[4:5], 0, v[136:137]
	global_load_lds_dwordx4 v[0:1], off
	v_lshl_add_u64 v[0:1], s[4:5], 0, v[26:27]
	s_add_i32 m0, s3, 0x1e000
	v_lshlrev_b32_e32 v145, 14, v138
	global_load_lds_dwordx4 v[0:1], off
	v_and_b32_e32 v145, 0xffff8000, v145
	v_lshl_add_u32 v139, v139, 11, v145
	v_and_b32_e32 v138, 1, v138
	v_lshl_or_b32 v138, v138, 6, v139
	v_lshl_add_u32 v138, v143, 1, v138
	v_lshlrev_b32_e32 v143, 14, v140
	v_mov_b64_e32 v[134:135], v[30:31]
	v_mov_b64_e32 v[130:131], v[30:31]
	v_mov_b64_e32 v[118:119], v[30:31]
	v_mov_b64_e32 v[114:115], v[30:31]
	v_mov_b64_e32 v[102:103], v[30:31]
	v_mov_b64_e32 v[98:99], v[30:31]
	v_mov_b64_e32 v[86:87], v[30:31]
	v_mov_b64_e32 v[82:83], v[30:31]
	v_mov_b64_e32 v[126:127], v[30:31]
	v_mov_b64_e32 v[122:123], v[30:31]
	v_mov_b64_e32 v[110:111], v[30:31]
	v_mov_b64_e32 v[106:107], v[30:31]
	v_mov_b64_e32 v[94:95], v[30:31]
	v_mov_b64_e32 v[90:91], v[30:31]
	v_mov_b64_e32 v[78:79], v[30:31]
	v_mov_b64_e32 v[74:75], v[30:31]
	v_mov_b64_e32 v[70:71], v[30:31]
	v_mov_b64_e32 v[66:67], v[30:31]
	v_mov_b64_e32 v[54:55], v[30:31]
	v_mov_b64_e32 v[50:51], v[30:31]
	v_mov_b64_e32 v[38:39], v[30:31]
	v_mov_b64_e32 v[34:35], v[30:31]
	v_mov_b64_e32 v[12:13], v[28:29]
	v_mov_b64_e32 v[8:9], v[28:29]
	v_mov_b64_e32 v[62:63], v[30:31]
	v_mov_b64_e32 v[58:59], v[30:31]
	v_mov_b64_e32 v[46:47], v[30:31]
	v_mov_b64_e32 v[42:43], v[30:31]
	v_mov_b64_e32 v[20:21], v[28:29]
	v_mov_b64_e32 v[16:17], v[28:29]
	v_mov_b64_e32 v[4:5], v[28:29]
	v_mov_b64_e32 v[0:1], v[28:29]
	v_and_b32_e32 v143, 0xffff8000, v143
	v_mov_b64_e32 v[132:133], v[28:29]
	v_mov_b64_e32 v[128:129], v[28:29]
	v_mov_b64_e32 v[116:117], v[28:29]
	v_mov_b64_e32 v[112:113], v[28:29]
	v_mov_b64_e32 v[100:101], v[28:29]
	v_mov_b64_e32 v[96:97], v[28:29]
	v_mov_b64_e32 v[84:85], v[28:29]
	v_mov_b64_e32 v[80:81], v[28:29]
	v_mov_b64_e32 v[124:125], v[28:29]
	v_mov_b64_e32 v[120:121], v[28:29]
	v_mov_b64_e32 v[108:109], v[28:29]
	v_mov_b64_e32 v[104:105], v[28:29]
	v_mov_b64_e32 v[92:93], v[28:29]
	v_mov_b64_e32 v[88:89], v[28:29]
	v_mov_b64_e32 v[76:77], v[28:29]
	v_mov_b64_e32 v[72:73], v[28:29]
	v_mov_b64_e32 v[68:69], v[28:29]
	v_mov_b64_e32 v[64:65], v[28:29]
	v_mov_b64_e32 v[52:53], v[28:29]
	v_mov_b64_e32 v[48:49], v[28:29]
	v_mov_b64_e32 v[36:37], v[28:29]
	v_mov_b64_e32 v[32:33], v[28:29]
	v_mov_b64_e32 v[14:15], v[30:31]
	v_mov_b64_e32 v[10:11], v[30:31]
	v_mov_b64_e32 v[60:61], v[28:29]
	v_mov_b64_e32 v[56:57], v[28:29]
	v_mov_b64_e32 v[44:45], v[28:29]
	v_mov_b64_e32 v[40:41], v[28:29]
	v_mov_b64_e32 v[22:23], v[30:31]
	v_mov_b64_e32 v[18:19], v[30:31]
	v_mov_b64_e32 v[6:7], v[30:31]
	v_mov_b64_e32 v[2:3], v[30:31]
	v_lshl_add_u32 v141, v141, 11, v143
	v_and_b32_e32 v140, 1, v140
	s_waitcnt vmcnt(6)
	s_barrier
	s_nop 4
	v_lshl_or_b32 v140, v140, 6, v141
	v_mov_b32_e32 v139, v24
	v_lshl_add_u32 v140, v142, 1, v140
	v_mov_b32_e32 v141, v24
	v_lshl_add_u64 v[138:139], s[74:75], 0, v[138:139]
	v_lshl_add_u64 v[140:141], s[74:75], 0, v[140:141]
	s_mov_b32 s60, -2
	s_mov_b64 s[12:13], 0
	v_add_u32_e32 v142, 0, v144
	.p2align	6

;     __device__ __forceinline__ size_t aoff(const Unit& u) const { return (size_t)u.pm * BM * K * 2; }
;     __device__ __forceinline__ size_t aoff(const Unit& u) const { return (size_t)u.pm * BM * K * 2; }
;     ...
;         const char* nB = has_next ? nxt.B : cB; const char* nA = has_next ? Abase + S.aoff(nxt) : cA;
;         const bool fresh_nxt = !(AREUSE && has_next && nxt.e == cur.e && nxt.pm == cur.pm);
;         const bool ff = fresh_cur && fresh_nxt;
;     ...
;         for (int t = 0; t < nt; t += 2) {
.LBB0_431:
	s_and_b64 s[6:7], s[92:93], exec
	s_cselect_b32 s13, s73, s5
	s_cselect_b32 s63, s72, s4
	s_add_u32 s64, s4, 0x100
	s_addc_u32 s65, s5, 0
	s_mov_b32 s66, -2
	s_mov_b64 s[20:21], 0
	.p2align	6

; #define PG8_STAGE(bufoff, gbase, voff) do { _Pragma("unroll") for (int _i = 0; _i < 2; ++_i) \
;         __builtin_amdgcn_global_load_lds((const unsigned*)((const char*)(gbase) + (voff)[_i]), (LAS unsigned*)(lds + (bufoff) + ldsw + _i * 8192), 16, 0, 0); } while (0)
; #define PG8_STAGEA(bufoff, uptr, koff, NEXT, h) do { if constexpr (GATHER) { if (NEXT) { const u32x2 _t = *(const LAS u32x2*)(vnslot + 2 * (h)); unsigned _v[2] = {_t.x, _t.y}; PG8_STAGE(bufoff, Abase + (koff), _v); } else { PG8_STAGE(bufoff, Abase + (koff), vc[h]); } } \
;         else { PG8_STAGE(bufoff, (uptr) + (size_t)(h) * hstep + (koff), voffA); } } while (0)
; #define PG8_WAIT_L(n) asm volatile("s_waitcnt lgkmcnt(" #n ")" ::: "memory")
; #define PG8_BAR __builtin_amdgcn_s_barrier()
; #define PG8_SCHED __builtin_amdgcn_sched_barrier(0)
; #define PG8_WAITX do { if (!AREUSE || ff) PG8_WAIT_V(8); else PG8_WAIT_V(4); } while (0)
;     ...
;             PG8_LDA(At, 1, 1); PG8_STAGE(PG8_SB(1, 0), b3, voffB); PG8_STAGE(PG8_SB(1, 1), b3 + bhstep, voffB); if (!AREUSE || fresh_nxt) PG8_STAGEA(PG8_SA(1, 0), u2, k3, last, 0);
;             PG8_WAITX; PG8_WAIT_L(0); PG8_BAR; PG8_MMA(1, 0, At, B0); PG8_MMA(1, 1, At, B1); PG8_BAR; PG8_SCHED;
.LBB0_602:
	s_mov_b32 m0, s64
	s_nop 0
	global_load_lds_dwordx4 v[220:221], off
	s_waitcnt vmcnt(8)
	s_waitcnt lgkmcnt(0)
	s_barrier
	s_setprio 1
	s_waitcnt lgkmcnt(0)
	v_mfma_f32_16x16x128_f8f6f4 v[126:129], v[24:31], v[56:63], v[126:129]
	v_mfma_f32_16x16x128_f8f6f4 v[122:125], v[16:23], v[56:63], v[122:125]
	v_mfma_f32_16x16x128_f8f6f4 v[110:113], v[24:31], v[48:55], v[110:113]
	v_mfma_f32_16x16x128_f8f6f4 v[106:109], v[16:23], v[48:55], v[106:109]
	v_mfma_f32_16x16x128_f8f6f4 v[94:97], v[24:31], v[40:47], v[94:97]
	v_mfma_f32_16x16x128_f8f6f4 v[90:93], v[16:23], v[40:47], v[90:93]
	v_mfma_f32_16x16x128_f8f6f4 v[78:81], v[24:31], v[32:39], v[78:81]
	v_mfma_f32_16x16x128_f8f6f4 v[70:73], v[16:23], v[32:39], v[70:73]
	s_setprio 0
	s_setprio 1
	v_mfma_f32_16x16x128_f8f6f4 v[118:121], v[8:15], v[56:63], v[118:121]
	v_mfma_f32_16x16x128_f8f6f4 v[114:117], v[0:7], v[56:63], v[114:117]
	v_mfma_f32_16x16x128_f8f6f4 v[102:105], v[8:15], v[48:55], v[102:105]
	v_mfma_f32_16x16x128_f8f6f4 v[98:101], v[0:7], v[48:55], v[98:101]
	v_mfma_f32_16x16x128_f8f6f4 v[86:89], v[8:15], v[40:47], v[86:89]
	v_mfma_f32_16x16x128_f8f6f4 v[82:85], v[0:7], v[40:47], v[82:85]
	v_mfma_f32_16x16x128_f8f6f4 v[74:77], v[8:15], v[32:39], v[74:77]
	v_mfma_f32_16x16x128_f8f6f4 v[66:69], v[0:7], v[32:39], v[66:69]
	s_setprio 0
	s_barrier
	s_add_i32 s49, s49, 2
	s_cmp_gt_u32 s49, 5
	s_cbranch_scc1 .LBB0_615
	.p2align	6

;     __device__ __forceinline__ size_t aoff(const Unit& u) const { return (size_t)u.pm * BM * K * 2; }
;     __device__ __forceinline__ size_t aoff(const Unit& u) const { return (size_t)u.pm * BM * K * 2; }
;     ...
;         const char* nB = has_next ? nxt.B : cB; const char* nA = has_next ? Abase + S.aoff(nxt) : cA;
;         const bool fresh_nxt = !(AREUSE && has_next && nxt.e == cur.e && nxt.pm == cur.pm);
;         const bool ff = fresh_cur && fresh_nxt;
;     ...
;         for (int t = 0; t < nt; t += 2) {
.LBB0_645:
	s_add_u32 s18, s18, s0
	s_addc_u32 s19, s19, s51
	s_mov_b64 s[4:5], 0
	.p2align	6

;     ...
; #pragma unroll 1
;     for (int i2 = 1; i2 < n_it; i2 += 2) {
;         D2_PIECE(1, i2, true);
;         if (i2 + 1 < n_it) D2_PIECE(0, i2 + 1, true);
;     }
.LBB0_774:
	s_add_i32 s6, s6, 2
	s_cmp_ge_i32 s6, s25
	s_cbranch_scc1 .LBB0_755
	.p2align	6
